# v045 with the GEMM1 start stagger in 8 groups of s_sleep 64 instead of 4 groups of s_sleep 127
# speedup vs baseline: 1.0067x; 1.0014x over previous
.LBB0_1235:
	s_andn2_b64 vcc, exec, s[0:1]
	s_cbranch_vccnz .LBB0_1338
	s_cmp_lg_u32 s52, 3
	v_readlane_b32 s4, v253, 4
	s_cselect_b64 s[0:1], -1, 0
	v_readlane_b32 s5, v253, 5
	s_and_b64 s[0:1], s[4:5], s[0:1]
	v_readlane_b32 s4, v254, 32
	v_readlane_b32 s5, v254, 33
	s_and_b64 s[4:5], s[4:5], s[0:1]
	v_readlane_b32 s44, v253, 0
	v_readlane_b32 s45, v253, 1
	s_andn2_b64 vcc, exec, s[4:5]
	s_mov_b64 s[4:5], -1
	s_cbranch_vccz .LBB0_1258
	v_mov_b32_e32 v4, v0
	s_movk_i32 s5, 0x3c0
	v_readfirstlane_b32 s23, v4
	v_and_b32_e32 v2, 48, v4
	v_lshlrev_b32_e32 v3, 6, v4
	s_ashr_i32 s25, s23, 8
	v_and_or_b32 v2, v3, s5, v2
	v_lshlrev_b32_e32 v3, 2, v4
	s_ashr_i32 s24, s23, 6
	s_lshl_b32 s4, s25, 13
	v_and_b32_e32 v5, 32, v3
	v_bitop3_b32 v3, v2, s4, v5 bitop3:0xde
	s_lshl_b32 s4, s24, 5
	s_and_b32 s6, s4, 0x60
	s_lshl_b32 s4, s6, 7
	v_bitop3_b32 v2, s4, v2, v5 bitop3:0xf6
	v_readlane_b32 s4, v254, 34
	v_readlane_b32 s5, v254, 35
	v_or_b32_e32 v2, 0x10000, v2
	s_andn2_b64 vcc, exec, s[4:5]
	s_cbranch_vccnz .LBB0_1257
	s_cmp_lt_u32 s52, 3
	s_cbranch_scc0 .Lfz_nostag
	s_bfe_u32 s4, s88, 0x30003
	s_cmp_eq_u32 s4, 0
	s_cbranch_scc1 .Lfz_nostag
.Lfz_stag:
	s_sleep 64
	s_add_i32 s4, s4, -1
	s_cmp_lg_u32 s4, 0
	s_cbranch_scc1 .Lfz_stag
